# final combine with nt streaming loads/stores only (no P15 split), to separate the two effects
# baseline (speedup 1.0000x reference)
; __device__ __forceinline__ float bf_lo(unsigned w) { return __uint_as_float(w << 16); }
; __device__ __forceinline__ float bf_hi(unsigned w) { return __uint_as_float(w & 0xffff0000u); }
; __device__ __forceinline__ f32x4 ld4_bf(const bf16_t* p) { const u32x2 w = *(const u32x2*)p; return (f32x4){bf_lo(w.x), bf_hi(w.x), bf_lo(w.y), bf_hi(w.y)}; }
; __device__ __forceinline__ float sq4(const f32x4 v) { return (v[0] * v[0] + v[1] * v[1]) + (v[2] * v[2] + v[3] * v[3]); }
; __device__ __forceinline__ void phase_final(const Ctx& P, volatile LAS int* tab, int vcu, int G) {
;     ...
;     for (int row = gw; row < ML; row += NGW) {
;         const int e1 = tok[row * 8], pos1 = tok[row * 8 + 1], e2 = tok[row * 8 + 2], pos2 = tok[row * 8 + 3]; const float p1 = ((const float*)tok)[row * 8 + 4], p2 = ((const float*)tok)[row * 8 + 5];
;         const bf16_t* y1 = YB + (size_t)(tab[8 + e1] * 256 + pos1) * DM; const bf16_t* y2 = YB + (size_t)(tab[8 + e2] * 256 + pos2) * DM;
;         const bf16_t* xr = (const bf16_t*)(P.ws + WS_XA) + (size_t)row * DM; const float* g2 = mod + (size_t)(row >> 12) * NMOD + 5 * DM;
;         f32x4 v[8]; float ss = 0.f;
; #pragma unroll
;         for (int j = 0; j < 8; ++j) { const int c = 4 * lane + 256 * j; const f32x4 x4 = ld4_bf(xr + c), g4 = *(const f32x4*)(g2 + c); const u32x2 a = *(const u32x2*)(y1 + c), b = *(const u32x2*)(y2 + c);
;             const f32x4 ya = (f32x4){bf_lo(a.x), bf_hi(a.x), bf_lo(a.y), bf_hi(a.y)}, yb = (f32x4){bf_lo(b.x), bf_hi(b.x), bf_lo(b.y), bf_hi(b.y)};
;             v[j] = x4 + g4 * (ya * p1 + yb * p2); ss += sq4(v[j]); }
.LBB0_2712:
	v_mov_b32_e32 v16, v194
	v_mov_b32_e32 v17, v195
	v_mov_b32_e32 v18, v196
	v_mov_b32_e32 v19, v197
	v_mov_b32_e32 v46, v198
	v_mov_b32_e32 v47, v199
	s_ashr_i32 s3, s10, 12
	s_mul_hi_i32 s8, s3, 0xc000
	s_mul_i32 s3, s3, 0xc000
	s_add_u32 s3, s36, s3
	s_addc_u32 s9, s37, s8
	s_add_u32 s8, s3, 0x146000
	s_addc_u32 s9, s9, 0
	s_add_i32 s10, s10, s0
	s_add_i32 s2, s2, s13
	s_ashr_i32 s3, s2, 31
	s_lshl_b64 s[14:15], s[2:3], 2
	s_add_u32 s14, s11, s14
	s_addc_u32 s15, s12, s15
	s_cmpk_lt_i32 s10, 0x4000
	v_lshlrev_b32_e32 v0, 2, v16
	v_lshlrev_b32_e32 v1, 2, v18
	v_add_u32_e32 v0, s1, v0
	v_add_u32_e32 v1, s1, v1
	ds_read_b32 v16, v0 offset:32
	ds_read_b32 v18, v1 offset:32
	global_load_dwordx2 v[48:49], v[34:35], off offset:-2048 nt
	global_load_dwordx2 v[50:51], v[34:35], off offset:-1536 nt
	global_load_dwordx2 v[52:53], v[34:35], off offset:-1024 nt
	global_load_dwordx4 v[0:3], v28, s[8:9]
	global_load_dwordx2 v[54:55], v[34:35], off offset:-512 nt
	global_load_dwordx4 v[8:11], v64, s[8:9]
	global_load_dwordx4 v[4:7], v65, s[8:9]
	global_load_dwordx4 v[12:15], v66, s[8:9]
	global_load_dwordx2 v[56:57], v[34:35], off nt
	global_load_dwordx4 v[20:23], v36, s[8:9]
	global_load_dwordx4 v[24:27], v38, s[8:9]
	global_load_dwordx2 v[76:77], v[34:35], off offset:512 nt
	global_load_dwordx2 v[78:79], v[34:35], off offset:1024 nt
	global_load_dwordx2 v[80:81], v[34:35], off offset:1536 nt
	global_load_dwordx4 v[68:71], v40, s[8:9]
	global_load_dwordx4 v[72:75], v42, s[8:9]
	v_lshl_add_u64 v[34:35], v[34:35], 0, s[6:7]
	s_waitcnt lgkmcnt(0)
	v_lshlrev_b32_e32 v16, 8, v16
	v_lshlrev_b32_e32 v18, 8, v18
	v_add_u32_e32 v16, v16, v17
	v_add_u32_e32 v18, v18, v19
	v_ashrrev_i32_e32 v17, 31, v16
	v_ashrrev_i32_e32 v19, 31, v18
	v_lshlrev_b64 v[16:17], 12, v[16:17]
	v_lshlrev_b64 v[18:19], 12, v[18:19]
	v_lshl_add_u64 v[16:17], v[30:31], 0, v[16:17]
	v_lshl_add_u64 v[18:19], v[30:31], 0, v[18:19]
	global_load_dwordx2 v[84:85], v[16:17], off nt
	global_load_dwordx2 v[86:87], v[18:19], off nt
	global_load_dwordx2 v[88:89], v[16:17], off offset:512 nt
	global_load_dwordx2 v[90:91], v[18:19], off offset:512 nt
	global_load_dwordx2 v[92:93], v[16:17], off offset:1024 nt
	global_load_dwordx2 v[94:95], v[18:19], off offset:1024 nt
	global_load_dwordx2 v[96:97], v[16:17], off offset:1536 nt
	global_load_dwordx2 v[98:99], v[18:19], off offset:1536 nt
	global_load_dwordx2 v[100:101], v[16:17], off offset:2048 nt
	global_load_dwordx2 v[102:103], v[18:19], off offset:2048 nt
	global_load_dwordx2 v[104:105], v[16:17], off offset:2560 nt
	global_load_dwordx2 v[106:107], v[16:17], off offset:3072 nt
	global_load_dwordx2 v[108:109], v[16:17], off offset:3584 nt
	global_load_dwordx2 v[110:111], v[18:19], off offset:2560 nt
	global_load_dwordx2 v[112:113], v[18:19], off offset:3072 nt
	global_load_dwordx2 v[114:115], v[18:19], off offset:3584 nt
	global_load_dwordx4 v[194:197], v29, s[14:15]
	global_load_dwordx2 v[198:199], v29, s[14:15] offset:16
	s_waitcnt vmcnt(2)
	v_lshlrev_b32_e32 v116, 16, v48
	v_and_b32_e32 v117, 0xffff0000, v48
	v_lshlrev_b32_e32 v48, 16, v49
	v_and_b32_e32 v49, 0xffff0000, v49
	v_lshlrev_b32_e32 v118, 16, v50
	v_and_b32_e32 v119, 0xffff0000, v50
	v_lshlrev_b32_e32 v50, 16, v51
	v_and_b32_e32 v51, 0xffff0000, v51
	v_lshlrev_b32_e32 v120, 16, v52
	v_and_b32_e32 v121, 0xffff0000, v52
	v_lshlrev_b32_e32 v52, 16, v53
	v_and_b32_e32 v53, 0xffff0000, v53
	v_lshlrev_b32_e32 v124, 16, v56
	v_and_b32_e32 v125, 0xffff0000, v56
	v_lshlrev_b32_e32 v132, 16, v86
	v_and_b32_e32 v133, 0xffff0000, v86
	v_lshlrev_b32_e32 v86, 16, v87
	v_and_b32_e32 v87, 0xffff0000, v87
	v_lshlrev_b32_e32 v136, 16, v90
	v_and_b32_e32 v137, 0xffff0000, v90
	v_lshlrev_b32_e32 v90, 16, v91
	v_and_b32_e32 v91, 0xffff0000, v91
	v_lshlrev_b32_e32 v82, 16, v84
	v_and_b32_e32 v83, 0xffff0000, v84
	v_lshlrev_b32_e32 v84, 16, v85
	v_and_b32_e32 v85, 0xffff0000, v85
	v_lshlrev_b32_e32 v134, 16, v88
	v_and_b32_e32 v135, 0xffff0000, v88
	v_lshlrev_b32_e32 v88, 16, v89
	v_and_b32_e32 v89, 0xffff0000, v89
	v_lshlrev_b32_e32 v140, 16, v94
	v_and_b32_e32 v141, 0xffff0000, v94
	v_lshlrev_b32_e32 v94, 16, v95
	v_and_b32_e32 v95, 0xffff0000, v95
	v_lshlrev_b32_e32 v148, 16, v102
	v_and_b32_e32 v149, 0xffff0000, v102
	v_lshlrev_b32_e32 v102, 16, v103
	v_and_b32_e32 v103, 0xffff0000, v103
	v_lshlrev_b32_e32 v156, 16, v112
	v_and_b32_e32 v157, 0xffff0000, v112
	v_lshlrev_b32_e32 v112, 16, v113
	v_and_b32_e32 v113, 0xffff0000, v113
	v_pk_mul_f32 v[86:87], v[46:47], v[86:87] op_sel:[1,0]
	v_pk_mul_f32 v[132:133], v[46:47], v[132:133] op_sel:[1,0]
	v_pk_mul_f32 v[90:91], v[46:47], v[90:91] op_sel:[1,0]
	v_pk_mul_f32 v[136:137], v[46:47], v[136:137] op_sel:[1,0]
	v_lshlrev_b32_e32 v138, 16, v92
	v_and_b32_e32 v139, 0xffff0000, v92
	v_lshlrev_b32_e32 v92, 16, v93
	v_and_b32_e32 v93, 0xffff0000, v93
	v_lshlrev_b32_e32 v144, 16, v98
	v_and_b32_e32 v145, 0xffff0000, v98
	v_lshlrev_b32_e32 v98, 16, v99
	v_and_b32_e32 v99, 0xffff0000, v99
	v_lshlrev_b32_e32 v146, 16, v100
	v_and_b32_e32 v147, 0xffff0000, v100
	v_lshlrev_b32_e32 v100, 16, v101
	v_and_b32_e32 v101, 0xffff0000, v101
	v_lshlrev_b32_e32 v152, 16, v110
	v_and_b32_e32 v153, 0xffff0000, v110
	v_lshlrev_b32_e32 v110, 16, v111
	v_and_b32_e32 v111, 0xffff0000, v111
	v_lshlrev_b32_e32 v154, 16, v106
	v_and_b32_e32 v155, 0xffff0000, v106
	v_lshlrev_b32_e32 v106, 16, v107
	v_and_b32_e32 v107, 0xffff0000, v107
	v_lshlrev_b32_e32 v160, 16, v114
	v_and_b32_e32 v161, 0xffff0000, v114
	v_lshlrev_b32_e32 v114, 16, v115
	v_and_b32_e32 v115, 0xffff0000, v115
	v_pk_mul_f32 v[140:141], v[46:47], v[140:141] op_sel:[1,0]
	v_pk_mul_f32 v[94:95], v[46:47], v[94:95] op_sel:[1,0]
; __device__ __forceinline__ float bf_lo(unsigned w) { return __uint_as_float(w << 16); }
; __device__ __forceinline__ float bf_hi(unsigned w) { return __uint_as_float(w & 0xffff0000u); }
; __device__ __forceinline__ f32x4 ld4_bf(const bf16_t* p) { const u32x2 w = *(const u32x2*)p; return (f32x4){bf_lo(w.x), bf_hi(w.x), bf_lo(w.y), bf_hi(w.y)}; }
; __device__ __forceinline__ float sq4(const f32x4 v) { return (v[0] * v[0] + v[1] * v[1]) + (v[2] * v[2] + v[3] * v[3]); }
; __device__ __forceinline__ void phase_final(const Ctx& P, volatile LAS int* tab, int vcu, int G) {
;     ...
; #pragma unroll
;         for (int j = 0; j < 8; ++j) { const int c = 4 * lane + 256 * j; const f32x4 x4 = ld4_bf(xr + c), g4 = *(const f32x4*)(g2 + c); const u32x2 a = *(const u32x2*)(y1 + c), b = *(const u32x2*)(y2 + c);
;             const f32x4 ya = (f32x4){bf_lo(a.x), bf_hi(a.x), bf_lo(a.y), bf_hi(a.y)}, yb = (f32x4){bf_lo(b.x), bf_hi(b.x), bf_lo(b.y), bf_hi(b.y)};
;             v[j] = x4 + g4 * (ya * p1 + yb * p2); ss += sq4(v[j]); }
;         ss = wave_sum(ss); const float rstd = __builtin_amdgcn_rsqf(ss * (1.0f / DM) + EPS);
	v_pk_mul_f32 v[102:103], v[46:47], v[102:103] op_sel:[1,0]
	v_pk_mul_f32 v[112:113], v[46:47], v[112:113] op_sel:[1,0]
	v_pk_fma_f32 v[82:83], v[46:47], v[82:83], v[132:133] op_sel_hi:[0,1,1]
	v_pk_fma_f32 v[84:85], v[46:47], v[84:85], v[86:87] op_sel_hi:[0,1,1]
	v_pk_fma_f32 v[86:87], v[46:47], v[134:135], v[136:137] op_sel_hi:[0,1,1]
	v_pk_fma_f32 v[88:89], v[46:47], v[88:89], v[90:91] op_sel_hi:[0,1,1]
	v_lshlrev_b32_e32 v56, 16, v57
	v_and_b32_e32 v57, 0xffff0000, v57
	v_lshlrev_b32_e32 v128, 16, v78
	v_and_b32_e32 v129, 0xffff0000, v78
	v_lshlrev_b32_e32 v78, 16, v79
	v_and_b32_e32 v79, 0xffff0000, v79
	v_lshlrev_b32_e32 v142, 16, v96
	v_and_b32_e32 v143, 0xffff0000, v96
	v_lshlrev_b32_e32 v96, 16, v97
	v_and_b32_e32 v97, 0xffff0000, v97
	v_lshlrev_b32_e32 v150, 16, v104
	v_and_b32_e32 v151, 0xffff0000, v104
	v_lshlrev_b32_e32 v104, 16, v105
	v_and_b32_e32 v105, 0xffff0000, v105
	v_lshlrev_b32_e32 v158, 16, v108
	v_and_b32_e32 v159, 0xffff0000, v108
	v_lshlrev_b32_e32 v108, 16, v109
	v_and_b32_e32 v109, 0xffff0000, v109
	v_pk_mul_f32 v[98:99], v[46:47], v[98:99] op_sel:[1,0]
	v_pk_mul_f32 v[144:145], v[46:47], v[144:145] op_sel:[1,0]
	v_pk_mul_f32 v[148:149], v[46:47], v[148:149] op_sel:[1,0]
	v_pk_mul_f32 v[152:153], v[46:47], v[152:153] op_sel:[1,0]
	v_pk_mul_f32 v[110:111], v[46:47], v[110:111] op_sel:[1,0]
	v_pk_mul_f32 v[156:157], v[46:47], v[156:157] op_sel:[1,0]
	v_pk_mul_f32 v[114:115], v[46:47], v[114:115] op_sel:[1,0]
	v_pk_mul_f32 v[160:161], v[46:47], v[160:161] op_sel:[1,0]
	v_pk_fma_f32 v[90:91], v[46:47], v[92:93], v[94:95] op_sel_hi:[0,1,1]
	v_pk_fma_f32 v[92:93], v[46:47], v[138:139], v[140:141] op_sel_hi:[0,1,1]
	v_pk_fma_f32 v[100:101], v[46:47], v[100:101], v[102:103] op_sel_hi:[0,1,1]
	v_pk_fma_f32 v[106:107], v[46:47], v[106:107], v[112:113] op_sel_hi:[0,1,1]
	v_pk_fma_f32 v[2:3], v[2:3], v[84:85], v[48:49]
	v_pk_fma_f32 v[0:1], v[0:1], v[82:83], v[116:117]
	v_pk_fma_f32 v[10:11], v[10:11], v[88:89], v[50:51]
	v_pk_fma_f32 v[8:9], v[8:9], v[86:87], v[118:119]
	v_lshlrev_b32_e32 v122, 16, v54
	v_and_b32_e32 v123, 0xffff0000, v54
	v_lshlrev_b32_e32 v54, 16, v55
	v_and_b32_e32 v55, 0xffff0000, v55
	v_lshlrev_b32_e32 v130, 16, v80
	v_and_b32_e32 v131, 0xffff0000, v80
	v_lshlrev_b32_e32 v80, 16, v81
	v_and_b32_e32 v81, 0xffff0000, v81
	v_pk_fma_f32 v[94:95], v[46:47], v[142:143], v[144:145] op_sel_hi:[0,1,1]
	v_pk_fma_f32 v[96:97], v[46:47], v[96:97], v[98:99] op_sel_hi:[0,1,1]
	v_pk_fma_f32 v[98:99], v[46:47], v[146:147], v[148:149] op_sel_hi:[0,1,1]
	v_pk_fma_f32 v[102:103], v[46:47], v[104:105], v[110:111] op_sel_hi:[0,1,1]
	v_pk_fma_f32 v[104:105], v[46:47], v[150:151], v[152:153] op_sel_hi:[0,1,1]
	v_pk_fma_f32 v[110:111], v[46:47], v[154:155], v[156:157] op_sel_hi:[0,1,1]
	v_pk_fma_f32 v[112:113], v[46:47], v[158:159], v[160:161] op_sel_hi:[0,1,1]
	v_pk_fma_f32 v[46:47], v[46:47], v[108:109], v[114:115] op_sel_hi:[0,1,1]
	v_pk_fma_f32 v[4:5], v[4:5], v[92:93], v[120:121]
	v_pk_fma_f32 v[6:7], v[6:7], v[90:91], v[52:53]
	v_pk_fma_f32 v[22:23], v[22:23], v[100:101], v[56:57]
	v_pk_fma_f32 v[48:49], v[70:71], v[106:107], v[78:79]
	v_mov_b32_e32 v56, v1
	v_mov_b32_e32 v57, v9
	v_mov_b32_e32 v70, v3
	v_mov_b32_e32 v71, v11
	v_pk_fma_f32 v[14:15], v[14:15], v[96:97], v[54:55]
	v_pk_fma_f32 v[50:51], v[68:69], v[110:111], v[128:129]
	v_pk_fma_f32 v[46:47], v[74:75], v[46:47], v[80:81]
	v_pk_fma_f32 v[52:53], v[72:73], v[112:113], v[130:131]
	v_mov_b32_e32 v54, v0
	v_mov_b32_e32 v55, v8
	v_mov_b32_e32 v68, v2
	v_mov_b32_e32 v69, v10
	v_pk_mul_f32 v[72:73], v[6:7], v[6:7]
	v_pk_mul_f32 v[74:75], v[4:5], v[4:5]
	v_pk_mul_f32 v[56:57], v[56:57], v[56:57]
	v_pk_mul_f32 v[70:71], v[70:71], v[70:71]
	v_lshlrev_b32_e32 v126, 16, v76
	v_and_b32_e32 v127, 0xffff0000, v76
	v_lshlrev_b32_e32 v76, 16, v77
	v_and_b32_e32 v77, 0xffff0000, v77
	v_pk_fma_f32 v[12:13], v[12:13], v[94:95], v[122:123]
	v_pk_mov_b32 v[88:89], v[74:75], v[72:73] op_sel:[1,0]
	v_mov_b32_e32 v75, v73
	v_pk_fma_f32 v[54:55], v[54:55], v[54:55], v[56:57]
	v_pk_fma_f32 v[56:57], v[68:69], v[68:69], v[70:71]
	v_pk_fma_f32 v[20:21], v[20:21], v[98:99], v[124:125]
	v_pk_fma_f32 v[26:27], v[26:27], v[102:103], v[76:77]
	v_mul_f32_e32 v76, v13, v13
	v_mul_f32_e32 v78, v15, v15
	v_pk_add_f32 v[68:69], v[88:89], v[74:75]
	v_pk_add_f32 v[54:55], v[54:55], v[56:57]
	v_pk_fma_f32 v[24:25], v[24:25], v[104:105], v[126:127]
	v_mul_f32_e32 v87, v20, v20
	v_mul_f32_e32 v90, v21, v21
	v_mul_f32_e32 v91, v22, v22
	v_mul_f32_e32 v92, v23, v23
	v_pk_fma_f32 v[72:73], v[12:13], v[12:13], v[76:77] op_sel_hi:[1,1,0]
	v_pk_fma_f32 v[76:77], v[14:15], v[14:15], v[78:79] op_sel_hi:[1,1,0]
	v_pk_add_f32 v[56:57], v[68:69], v[68:69] op_sel:[0,1] op_sel_hi:[1,0]
	v_pk_add_f32 v[54:55], v[54:55], v[54:55] op_sel:[0,1] op_sel_hi:[1,0]
	v_pk_mul_f32 v[80:81], v[26:27], v[26:27]
	v_pk_mul_f32 v[82:83], v[24:25], v[24:25]
	v_mov_b32_e32 v73, v91
	v_mov_b32_e32 v77, v92
	v_mov_b32_e32 v57, v90
	v_mov_b32_e32 v55, v87
	v_pk_mov_b32 v[78:79], v[82:83], v[80:81] op_sel:[1,0]
	v_mov_b32_e32 v83, v81
	v_pk_add_f32 v[68:69], v[72:73], v[76:77]
	v_pk_add_f32 v[54:55], v[54:55], v[56:57]
	v_mul_f32_e32 v84, v51, v51
	v_mul_f32_e32 v86, v49, v49
	v_pk_add_f32 v[70:71], v[78:79], v[82:83]
	v_pk_add_f32 v[54:55], v[54:55], v[68:69]
	v_mul_f32_e32 v93, v52, v52
	v_mul_f32_e32 v94, v53, v53
	v_mul_f32_e32 v95, v46, v46
	v_mul_f32_e32 v96, v47, v47
	v_pk_fma_f32 v[80:81], v[50:51], v[50:51], v[84:85] op_sel_hi:[1,1,0]
	v_pk_fma_f32 v[84:85], v[48:49], v[48:49], v[86:87] op_sel_hi:[1,1,0]
	v_pk_add_f32 v[70:71], v[70:71], v[70:71] op_sel:[0,1] op_sel_hi:[1,0]
	v_pk_add_f32 v[54:55], v[54:55], v[54:55] op_sel:[0,1] op_sel_hi:[1,0]
	v_mov_b32_e32 v81, v95
	v_mov_b32_e32 v85, v96
	v_mov_b32_e32 v71, v94
	v_mov_b32_e32 v55, v93
	v_pk_add_f32 v[72:73], v[80:81], v[84:85]
	v_pk_add_f32 v[54:55], v[54:55], v[70:71]
	s_nop 0
	v_pk_add_f32 v[54:55], v[54:55], v[72:73]
	s_nop 0
	v_add_f32_e32 v54, v54, v55
	ds_bpermute_b32 v55, v58, v54
	s_waitcnt lgkmcnt(0)
; __device__ __forceinline__ void phase_final(const Ctx& P, volatile LAS int* tab, int vcu, int G) {
;     ...
;         ss = wave_sum(ss); const float rstd = __builtin_amdgcn_rsqf(ss * (1.0f / DM) + EPS);
; #pragma unroll
;         for (int j = 0; j < 8; ++j) { const int c = 4 * lane + 256 * j; const f32x4 fg = *(const f32x4*)(P.in[34] + c); *(f32x4*)(P.out + (size_t)row * DM + c) = v[j] * rstd * fg; }
;     }
	v_add_f32_e32 v54, v54, v55
	ds_bpermute_b32 v55, v59, v54
	s_waitcnt lgkmcnt(0)
	v_add_f32_e32 v54, v54, v55
	ds_bpermute_b32 v55, v60, v54
	s_waitcnt lgkmcnt(0)
	v_add_f32_e32 v54, v54, v55
	ds_bpermute_b32 v55, v61, v54
	s_waitcnt lgkmcnt(0)
	v_add_f32_e32 v54, v54, v55
	ds_bpermute_b32 v55, v62, v54
	s_waitcnt lgkmcnt(0)
	v_add_f32_e32 v54, v54, v55
	ds_bpermute_b32 v55, v63, v54
	s_waitcnt lgkmcnt(0)
	v_add_f32_e32 v54, v54, v55
	v_fmamk_f32 v54, v54, 0x3a000000, v67
	v_rsq_f32_e32 v54, v54
	s_nop 0
	v_pk_mul_f32 v[0:1], v[0:1], v[54:55] op_sel_hi:[1,0]
	v_pk_mul_f32 v[2:3], v[2:3], v[54:55] op_sel_hi:[1,0]
	v_pk_mul_f32 v[8:9], v[8:9], v[54:55] op_sel_hi:[1,0]
	v_pk_mul_f32 v[10:11], v[10:11], v[54:55] op_sel_hi:[1,0]
	v_pk_mul_f32 v[4:5], v[4:5], v[54:55] op_sel_hi:[1,0]
	v_pk_mul_f32 v[6:7], v[6:7], v[54:55] op_sel_hi:[1,0]
	v_pk_mul_f32 v[12:13], v[12:13], v[54:55] op_sel_hi:[1,0]
	v_pk_mul_f32 v[14:15], v[14:15], v[54:55] op_sel_hi:[1,0]
	v_pk_mul_f32 v[20:21], v[20:21], v[54:55] op_sel_hi:[1,0]
	v_pk_mul_f32 v[22:23], v[22:23], v[54:55] op_sel_hi:[1,0]
	v_pk_mul_f32 v[24:25], v[24:25], v[54:55] op_sel_hi:[1,0]
	v_pk_mul_f32 v[26:27], v[26:27], v[54:55] op_sel_hi:[1,0]
	v_pk_mul_f32 v[68:69], v[50:51], v[54:55] op_sel_hi:[1,0]
	v_pk_mul_f32 v[70:71], v[48:49], v[54:55] op_sel_hi:[1,0]
	v_pk_mul_f32 v[72:73], v[52:53], v[54:55] op_sel_hi:[1,0]
	v_pk_mul_f32 v[74:75], v[46:47], v[54:55] op_sel_hi:[1,0]
	v_pk_mul_f32 v[0:1], v[162:163], v[0:1]
	v_pk_mul_f32 v[2:3], v[164:165], v[2:3]
	global_store_dwordx4 v[32:33], v[0:3], off offset:-4096 nt
	v_pk_mul_f32 v[8:9], v[166:167], v[8:9]
	v_pk_mul_f32 v[10:11], v[168:169], v[10:11]
	global_store_dwordx4 v[32:33], v[8:11], off offset:-3072 nt
	v_pk_mul_f32 v[4:5], v[170:171], v[4:5]
	v_pk_mul_f32 v[6:7], v[172:173], v[6:7]
	global_store_dwordx4 v[32:33], v[4:7], off offset:-2048 nt
	v_pk_mul_f32 v[12:13], v[174:175], v[12:13]
	v_pk_mul_f32 v[14:15], v[176:177], v[14:15]
	global_store_dwordx4 v[32:33], v[12:15], off offset:-1024 nt
	v_pk_mul_f32 v[20:21], v[178:179], v[20:21]
	v_pk_mul_f32 v[22:23], v[180:181], v[22:23]
	global_store_dwordx4 v[32:33], v[20:23], off nt
	v_pk_mul_f32 v[24:25], v[182:183], v[24:25]
	v_pk_mul_f32 v[26:27], v[184:185], v[26:27]
	global_store_dwordx4 v[32:33], v[24:27], off offset:1024 nt
	v_pk_mul_f32 v[68:69], v[186:187], v[68:69]
	v_pk_mul_f32 v[70:71], v[188:189], v[70:71]
	global_store_dwordx4 v[32:33], v[68:71], off offset:2048 nt
	v_pk_mul_f32 v[72:73], v[190:191], v[72:73]
	v_pk_mul_f32 v[74:75], v[192:193], v[74:75]
	global_store_dwordx4 v[32:33], v[72:75], off offset:3072 nt
	v_lshl_add_u64 v[32:33], v[32:33], 0, s[4:5]
	s_waitcnt vmcnt(8)
	s_cbranch_scc1 .LBB0_2712
